# speedup vs baseline: 1.0348x; 1.0005x over previous
_Z14headsum_kernelPKtPKfPjPf:
	s_load_dwordx2 s[4:5], s[0:1], 0x0
	s_load_dwordx2 s[12:13], s[0:1], 0x8
	s_mov_b32 s3, 0
	s_cmp_lg_u32 s2, 0
	v_mov_b32_e32 v69, 0
	s_cbranch_scc1 .LBB1_2
	s_load_dwordx2 s[6:7], s[0:1], 0x10
	v_lshlrev_b32_e32 v1, 2, v0
	s_waitcnt lgkmcnt(0)
	global_store_dword v1, v69, s[6:7]
	global_store_dword v1, v69, s[6:7] offset:1024
	global_store_dword v1, v69, s[6:7] offset:2048
	global_store_dword v1, v69, s[6:7] offset:3072
.LBB1_2:
	s_lshl_b64 s[8:9], s[2:3], 8
	s_lshr_b64 s[6:7], s[8:9], 11
	s_and_b32 s2, s6, 0x1ffffff0
	v_or_b32_e32 v66, s8, v0
	s_lshl_b64 s[10:11], s[2:3], 19
	v_and_b32_e32 v1, 0x7fff, v66
	s_waitcnt lgkmcnt(0)
	v_and_b32_e32 v82, 31, v0
	v_lshlrev_b32_e32 v82, 4, v82
	v_lshrrev_b32_e32 v83, 5, v0
	v_lshl_or_b32 v80, v83, 13, v82
	v_lshl_or_b32 v81, v83, 9, v82
	s_lshl_b32 s14, s2, 12
	s_sub_u32 s12, s12, 0x20000
	s_subb_u32 s13, s13, 0
	s_add_u32 s12, s12, s14
	s_addc_u32 s13, s13, 0
	s_add_u32 s14, s12, 0x1000
	s_addc_u32 s15, s13, 0
	global_load_dwordx4 v[88:91], v80, s[12:13] offset:0
	global_load_dwordx4 v[92:95], v80, s[12:13] offset:512
	global_load_dwordx4 v[96:99], v80, s[12:13] offset:1024
	global_load_dwordx4 v[100:103], v80, s[12:13] offset:1536
	global_load_dwordx4 v[104:107], v80, s[12:13] offset:2048
	global_load_dwordx4 v[108:111], v80, s[12:13] offset:2560
	global_load_dwordx4 v[112:115], v80, s[12:13] offset:3072
	global_load_dwordx4 v[116:119], v80, s[12:13] offset:3584
	global_load_dwordx4 v[120:123], v80, s[14:15] offset:0
	global_load_dwordx4 v[124:127], v80, s[14:15] offset:512
	global_load_dwordx4 v[128:131], v80, s[14:15] offset:1024
	global_load_dwordx4 v[132:135], v80, s[14:15] offset:1536
	global_load_dwordx4 v[136:139], v80, s[14:15] offset:2048
	global_load_dwordx4 v[140:143], v80, s[14:15] offset:2560
	global_load_dwordx4 v[144:147], v80, s[14:15] offset:3072
	global_load_dwordx4 v[148:151], v80, s[14:15] offset:3584
	s_add_u32 s4, s4, s10
	s_addc_u32 s5, s5, s11
	v_lshlrev_b32_e32 v68, 4, v1
	v_lshl_add_u64 v[14:15], s[4:5], 0, v[68:69]
	s_mov_b32 s8, 0x80000
	v_add_co_u32_e32 v2, vcc, s8, v14
	s_mov_b32 s8, 0x100000
	s_nop 0
	v_addc_co_u32_e32 v3, vcc, 0, v15, vcc
	v_add_co_u32_e32 v4, vcc, s8, v14
	s_mov_b32 s8, 0x180000
	s_nop 0
	v_addc_co_u32_e32 v5, vcc, 0, v15, vcc
	global_load_dwordx4 v[42:45], v[2:3], off
	global_load_dwordx4 v[34:37], v[4:5], off
	v_add_co_u32_e32 v2, vcc, s8, v14
	s_mov_b32 s8, 0x200000
	s_nop 0
	v_addc_co_u32_e32 v3, vcc, 0, v15, vcc
	v_add_co_u32_e32 v4, vcc, s8, v14
	s_mov_b32 s8, 0x280000
	s_nop 0
	v_addc_co_u32_e32 v5, vcc, 0, v15, vcc
	global_load_dwordx4 v[58:61], v[2:3], off
	global_load_dwordx4 v[46:49], v[4:5], off
	v_add_co_u32_e32 v2, vcc, s8, v14
	s_mov_b32 s8, 0x300000
	s_nop 0
	v_addc_co_u32_e32 v3, vcc, 0, v15, vcc
	v_add_co_u32_e32 v4, vcc, s8, v14
	s_mov_b32 s8, 0x380000
	s_nop 0
	v_addc_co_u32_e32 v5, vcc, 0, v15, vcc
	v_add_co_u32_e32 v6, vcc, s8, v14
	s_mov_b32 s8, 0x400000
	s_nop 0
	v_addc_co_u32_e32 v7, vcc, 0, v15, vcc
	v_add_co_u32_e32 v8, vcc, s8, v14
	s_mov_b32 s8, 0x480000
	s_nop 0
	v_addc_co_u32_e32 v9, vcc, 0, v15, vcc
	v_add_co_u32_e32 v16, vcc, s8, v14
	s_mov_b32 s8, 0x500000
	s_nop 0
	v_addc_co_u32_e32 v17, vcc, 0, v15, vcc
	v_add_co_u32_e32 v18, vcc, s8, v14
	s_mov_b32 s8, 0x580000
	s_nop 0
	v_addc_co_u32_e32 v19, vcc, 0, v15, vcc
	v_add_co_u32_e32 v70, vcc, s8, v14
	s_mov_b32 s8, 0x600000
	s_nop 0
	v_addc_co_u32_e32 v71, vcc, 0, v15, vcc
	v_add_co_u32_e32 v72, vcc, s8, v14
	s_mov_b32 s8, 0x680000
	s_nop 0
	v_addc_co_u32_e32 v73, vcc, 0, v15, vcc
	v_add_co_u32_e32 v74, vcc, s8, v14
	global_load_dwordx4 v[54:57], v[2:3], off
	global_load_dwordx4 v[38:41], v[4:5], off
	v_addc_co_u32_e32 v75, vcc, 0, v15, vcc
	v_add_co_u32_e32 v76, vcc, 0x700000, v14
	global_load_dwordx4 v[50:53], v[6:7], off
	global_load_dwordx4 v[2:5], v[8:9], off
	v_addc_co_u32_e32 v77, vcc, 0, v15, vcc
	v_add_co_u32_e32 v78, vcc, 0x780000, v14
	global_load_dwordx4 v[10:13], v[16:17], off
	global_load_dwordx4 v[6:9], v[18:19], off
	v_addc_co_u32_e32 v79, vcc, 0, v15, vcc
	global_load_dwordx4 v[30:33], v[70:71], off
	global_load_dwordx4 v[22:25], v[72:73], off
	global_load_dwordx4 v[26:29], v[74:75], off
	global_load_dwordx4 v[18:21], v[76:77], off
	global_load_dwordx4 v[62:65], v68, s[4:5]
	global_load_dwordx4 v[14:17], v[78:79], off
	s_load_dwordx2 s[4:5], s[0:1], 0x18
	v_mov_b32_e32 v67, s9
	s_waitcnt lgkmcnt(0)
	s_waitcnt vmcnt(31)
	s_waitcnt vmcnt(30)
	v_pk_add_f32 v[88:89], v[88:89], v[92:93]
	v_pk_add_f32 v[90:91], v[90:91], v[94:95]
	s_waitcnt vmcnt(29)
	v_pk_add_f32 v[88:89], v[88:89], v[96:97]
	v_pk_add_f32 v[90:91], v[90:91], v[98:99]
	s_waitcnt vmcnt(28)
	v_pk_add_f32 v[88:89], v[88:89], v[100:101]
	v_pk_add_f32 v[90:91], v[90:91], v[102:103]
	s_waitcnt vmcnt(27)
	v_pk_add_f32 v[88:89], v[88:89], v[104:105]
	v_pk_add_f32 v[90:91], v[90:91], v[106:107]
	s_waitcnt vmcnt(26)
	v_pk_add_f32 v[88:89], v[88:89], v[108:109]
	v_pk_add_f32 v[90:91], v[90:91], v[110:111]
	s_waitcnt vmcnt(25)
	v_pk_add_f32 v[88:89], v[88:89], v[112:113]
	v_pk_add_f32 v[90:91], v[90:91], v[114:115]
	s_waitcnt vmcnt(24)
	v_pk_add_f32 v[88:89], v[88:89], v[116:117]
	v_pk_add_f32 v[90:91], v[90:91], v[118:119]
	s_waitcnt vmcnt(23)
	v_pk_add_f32 v[88:89], v[88:89], v[120:121]
	v_pk_add_f32 v[90:91], v[90:91], v[122:123]
	s_waitcnt vmcnt(22)
	v_pk_add_f32 v[88:89], v[88:89], v[124:125]
	v_pk_add_f32 v[90:91], v[90:91], v[126:127]
	s_waitcnt vmcnt(21)
	v_pk_add_f32 v[88:89], v[88:89], v[128:129]
	v_pk_add_f32 v[90:91], v[90:91], v[130:131]
	s_waitcnt vmcnt(20)
	v_pk_add_f32 v[88:89], v[88:89], v[132:133]
	v_pk_add_f32 v[90:91], v[90:91], v[134:135]
	s_waitcnt vmcnt(19)
	v_pk_add_f32 v[88:89], v[88:89], v[136:137]
	v_pk_add_f32 v[90:91], v[90:91], v[138:139]
	s_waitcnt vmcnt(18)
	v_pk_add_f32 v[88:89], v[88:89], v[140:141]
	v_pk_add_f32 v[90:91], v[90:91], v[142:143]
	s_waitcnt vmcnt(17)
	v_pk_add_f32 v[88:89], v[88:89], v[144:145]
	v_pk_add_f32 v[90:91], v[90:91], v[146:147]
	s_waitcnt vmcnt(16)
	v_pk_add_f32 v[88:89], v[88:89], v[148:149]
	v_pk_add_f32 v[90:91], v[90:91], v[150:151]
	ds_write_b128 v81, v[88:91] offset:512
	s_waitcnt lgkmcnt(0)
	s_barrier
	s_movk_i32 s8, 0x80
	v_cmp_gt_u32_e32 vcc, s8, v0
	s_and_saveexec_b64 s[8:9], vcc
	s_cbranch_execz .LBB1_4
	v_lshlrev_b32_e32 v68, 2, v0
	ds_read_b32 v74, v68 offset:512
	ds_read_b32 v75, v68 offset:1024
	ds_read_b32 v76, v68 offset:1536
	ds_read_b32 v77, v68 offset:2048
	ds_read_b32 v78, v68 offset:2560
	ds_read_b32 v79, v68 offset:3072
	ds_read_b32 v80, v68 offset:3584
	ds_read_b32 v81, v68 offset:4096
	s_waitcnt lgkmcnt(0)
	v_add_f32_e32 v1, 0, v74
	v_add_f32_e32 v1, v1, v75
	v_add_f32_e32 v1, v1, v76
	v_add_f32_e32 v1, v1, v77
	v_add_f32_e32 v1, v1, v78
	v_add_f32_e32 v1, v1, v79
	v_add_f32_e32 v1, v1, v80
	v_add_f32_e32 v1, v1, v81
	v_mul_f32_e32 v1, 0x3bf00000, v1
	ds_write_b32 v68, v1
